# v4 + 4-byte code shift (instruction stream placement)
# baseline (speedup 1.0000x reference)
; __global__ void __launch_bounds__(NWAVES * 64, 2) fwd(Args args) {
;     ...
;     const int tid = threadIdx.x, lane = tid & 63, wave = __builtin_amdgcn_readfirstlane(tid >> 6);
;     const int G = gridDim.x; const int bx = blockIdx.x; const int vcu = (G % 8 == 0) ? (bx % 8) * (G / 8) + bx / 8 : bx;
_Z3fwd4Args:
	s_nop 0
	s_mov_b32 s96, s2
	s_load_dword s2, s[0:1], 0x90
	s_load_dwordx4 s[8:11], s[0:1], 0x80
	s_add_u32 s4, s0, 0x90
	s_addc_u32 s5, s1, 0
	v_readfirstlane_b32 s63, v0
	v_writelane_b32 v251, s4, 0
	s_mov_b32 s3, s96
	s_nop 0
	v_writelane_b32 v251, s5, 1
	s_waitcnt lgkmcnt(0)
	v_writelane_b32 v251, s2, 2
	s_and_b32 s2, s2, 7
	s_cmp_lg_u32 s2, 0
	s_cbranch_scc1 .LBB0_2
	s_load_dword s2, s[0:1], 0x90
	s_ashr_i32 s3, s96, 31
	s_lshr_b32 s3, s3, 29
	s_add_i32 s3, s96, s3
	s_and_b32 s4, s3, -8
	s_waitcnt lgkmcnt(0)
	s_ashr_i32 s2, s2, 3
	s_sub_i32 s4, s96, s4
	s_mul_i32 s2, s2, s4
	s_ashr_i32 s3, s3, 3
	s_add_i32 s3, s2, s3
